# code placement: attention loop head 64B-aligned and no 8-byte instruction straddles a 32-byte fetch boundary (e32->e64 promotion of VALU encodings)
# baseline (speedup 1.0000x reference)
.LBB0_733:
	s_or_b64 exec, exec, s[8:9]
	s_movk_i32 s4, 0xf0
	s_cmp_lg_u32 0, -1
	v_lshlrev_b32_e32 v39, 8, v141
	v_bitop3_b32 v80, v142, s4, v136 bitop3:0x48
	s_cselect_b32 s10, 0, 0
	v_cvt_pk_bf16_f32 v96, v134, v135
	v_cvt_pk_bf16_f32 v97, v132, v133
	v_cvt_pk_bf16_f32 v98, v130, v131
	v_cvt_pk_bf16_f32 v99, v128, v129
	v_cvt_pk_bf16_f32 v100, v126, v127
	v_cvt_pk_bf16_f32 v101, v124, v125
	v_cvt_pk_bf16_f32 v102, v122, v123
	v_cvt_pk_bf16_f32 v103, v120, v121
	v_cvt_pk_bf16_f32 v104, v70, v71
	v_cvt_pk_bf16_f32 v105, v74, v75
	v_cvt_pk_bf16_f32 v106, v64, v65
	v_cvt_pk_bf16_f32 v107, v68, v69
	v_cvt_pk_bf16_f32 v108, v60, v61
	v_cvt_pk_bf16_f32 v109, v66, v67
	v_cvt_pk_bf16_f32 v110, v56, v57
	v_cvt_pk_bf16_f32 v111, v58, v59
	v_cvt_pk_bf16_f32 v112, v112, v113
	v_cvt_pk_bf16_f32 v113, v118, v119
	v_cvt_pk_bf16_f32 v114, v114, v115
	v_cvt_pk_bf16_f32 v115, v116, v117
	v_cvt_pk_bf16_f32 v116, v78, v79
	v_cvt_pk_bf16_f32 v117, v76, v77
	v_cvt_pk_bf16_f32 v118, v72, v73
	v_cvt_pk_bf16_f32 v119, v62, v63
	v_cvt_pk_bf16_f32 v120, v52, v53
	v_cvt_pk_bf16_f32 v121, v54, v55
	v_cvt_pk_bf16_f32 v122, v46, v47
	v_cvt_pk_bf16_f32 v123, v50, v51
	v_cvt_pk_bf16_f32 v124, v44, v45
	v_cvt_pk_bf16_f32 v125, v48, v49
	v_cvt_pk_bf16_f32 v126, v40, v41
	v_cvt_pk_bf16_f32 v127, v42, v43
	v_readlane_b32 s100, v250, 8
	v_mbcnt_lo_u32_b32 v68, -1, 0
	v_mbcnt_hi_u32_b32 v68, -1, v68
	s_nop 1
	v_add_u32_e32 v69, s100, v68
	v_lshrrev_b32_e32 v70, 3, v69
	v_and_b32_e32 v71, 7, v69
	v_lshrrev_b32_e32 v72, 2, v71
	v_bfe_u32 v73, v71, 1, 1
	v_and_b32_e32 v74, 1, v71
	v_lshlrev_b32_e32 v74, 1, v74
	v_lshl_add_u32 v75, v72, 2, v74
	v_bfe_u32 v76, v70, 1, 3
	v_xor_b32_e32 v77, v75, v76
	v_add_u32_e32 v78, 1, v75
	v_xor_b32_e32 v78, v78, v76
	v_lshlrev_b32_e32 v79, 7, v70
	v_lshl_add_u32 v79, v73, 3, v79
	v_lshl_add_u32 v64, v77, 4, v79
	v_lshl_add_u32 v65, v78, 4, v79
	v_add_u32_e32 v66, 0x2000, v64
	v_add_u32_e32 v67, 0x2000, v65
	v_or_b32_e32 v81, v39, v80
	s_add_i32 s15, s10, 0x10000
	v_and_b32_e32 v82, 6, v137
	v_lshrrev_b32_e32 v84, 4, v136
	s_waitcnt vmcnt(0)
	s_waitcnt vmcnt(0)
	s_add_i32 s11, s10, 0x12000
	v_lshl_add_u32 v83, v139, 7, s10
	v_bitop3_b32 v85, v84, v82, 7 bitop3:0x6c
	v_and_b32_e32 v86, 8, v138
	v_or_b32_e32 v82, 1, v82
	v_add_u32_e32 v225, s15, v81
	s_waitcnt vmcnt(4)
	ds_write_b128 v225, v[24:27] offset:0
	v_lshlrev_b32_e32 v85, 4, v85
	v_add_u32_e32 v87, v83, v86
	v_bitop3_b32 v82, v84, v82, 7 bitop3:0x6c
	v_add3_u32 v226, v80, s11, v39
	ds_write_b128 v226, v[28:31] offset:0
	v_lshlrev_b32_e32 v82, 4, v82
	v_add_u32_e32 v227, v87, v85
	ds_write_b64 v64, v[12:13] offset:0
	v_lshrrev_b32_e32 v32, 5, v136
	v_add_u32_e32 v83, 0x2000, v83
	v_or_b32_e32 v84, v85, v86
	v_add_u32_e32 v228, v87, v82
	ds_write_b64 v65, v[14:15] offset:0
	v_xor_b32_e32 v32, v32, v137
	v_or_b32_e32 v86, v82, v86
	v_add_u32_e32 v229, v84, v83
	ds_write_b64 v66, v[4:5] offset:0
	v_lshlrev_b32_e32 v32, 4, v32
	v_add_u32_e32 v184, v86, v83
	ds_write_b64 v67, v[6:7] offset:0
	v_lshlrev_b32_e32 v33, 8, v143
	v_and_b32_e32 v32, 16, v32
	v_bfe_u32 v35, v137, 1, 3
	s_waitcnt vmcnt(4)
	ds_write_b128 v225, v[20:23] offset:0x4000
	v_lshlrev_b32_e32 v36, 5, v35
	v_add3_u32 v32, v33, s15, v32
	s_movk_i32 s16, 0x60
	ds_write_b128 v226, v[16:19] offset:0x4000
	v_xad_u32 v204, v36, s16, v32
	s_movk_i32 s16, 0x80
	ds_write_b64 v64, v[8:9] offset:0x4000
	v_xad_u32 v205, v36, s16, v32
	s_movk_i32 s16, 0xa0
	ds_write_b64 v65, v[10:11] offset:0x4000
	s_add_u32 s8, s6, 0x100
	v_xad_u32 v206, v36, s16, v32
	s_movk_i32 s16, 0xc0
	ds_write_b64 v66, v[0:1] offset:0x4000
	s_addc_u32 s9, s7, 0
	v_xad_u32 v207, v36, s16, v32
	s_movk_i32 s16, 0xe0
	ds_write_b64 v67, v[2:3] offset:0x4000
	v_add_u32_e32 v201, v32, v36
	v_xad_u32 v202, v36, 32, v32
	v_xad_u32 v203, v36, 64, v32
	v_xad_u32 v208, v36, s16, v32
	v_lshl_add_u32 v32, v143, 7, s10
	s_add_u32 s10, s78, 0x20000
	global_load_dwordx4 v[132:135], v198, s[8:9]
	s_addc_u32 s11, s79, 0
	global_load_dwordx4 v[128:131], v199, s[8:9]
	v_lshrrev_b32_e32 v34, 1, v137
	global_load_dwordx4 v[136:139], v196, s[10:11]
	s_add_u32 s6, s6, 0x180
	v_bitop3_b32 v34, v140, v34, 7 bitop3:0x78
	v_bitop3_b32 v37, v140, v35, 2 bitop3:0x36
	v_bitop3_b32 v38, v140, v35, 4 bitop3:0x36
	v_bitop3_b32 v35, v140, v35, 6 bitop3:0x36
	global_load_dwordx4 v[140:143], v197, s[10:11]
	s_addc_u32 s7, s7, 0
	s_add_u32 s8, s78, 0x30000
	global_load_dwordx4 v[148:151], v198, s[6:7]
	s_addc_u32 s9, s79, 0
	global_load_dwordx4 v[144:147], v199, s[6:7]
	global_load_dwordx4 v[152:155], v196, s[8:9]
	s_add_u32 s10, s13, s14
	global_load_dwordx4 v[156:159], v197, s[8:9]
	s_addc_u32 s11, s12, 0
	s_add_u32 s12, s41, s30
	v_mov_b32_e32 v0, 0
	s_mov_b32 s4, 0
	v_lshl_add_u32 v209, v34, 4, v32
	v_lshl_add_u32 v210, v37, 4, v32
	v_lshl_add_u32 v211, v38, 4, v32
	v_lshl_add_u32 v224, v35, 4, v32
	s_addc_u32 s13, 0, s31
	v_mov_b32_e32 v1, v0
	v_mov_b32_e32 v2, v0
	v_mov_b32_e32 v3, v0
	v_mov_b32_e32 v4, v0
	v_mov_b32_e32 v5, v0
	v_mov_b32_e32 v6, v0
	v_mov_b32_e32 v7, v0
	v_mov_b32_e32 v8, v0
	v_mov_b32_e32 v9, v0
	v_mov_b32_e32 v10, v0
	v_mov_b32_e32 v11, v0
	v_mov_b32_e32 v12, v0
	v_mov_b32_e32 v13, v0
	v_mov_b32_e32 v14, v0
	v_mov_b32_e32 v15, v0
	v_mov_b32_e32 v16, v0
	v_mov_b32_e32 v17, v0
	v_mov_b32_e32 v18, v0
	v_mov_b32_e32 v19, v0
	v_mov_b32_e32 v20, v0
	v_mov_b32_e32 v21, v0
	v_mov_b32_e32 v22, v0
	v_mov_b32_e32 v23, v0
	v_mov_b32_e32 v24, v0
	v_mov_b32_e32 v25, v0
	v_mov_b32_e32 v26, v0
	v_mov_b32_e32 v27, v0
	v_mov_b32_e32 v28, v0
	v_mov_b32_e32 v29, v0
	v_mov_b32_e32 v30, v0
	v_mov_b32_e32 v31, v0
	v_mov_b32_e32 v32, v0
	v_mov_b32_e32 v33, v0
	v_mov_b32_e32 v34, v0
	v_mov_b32_e32 v35, v0
	v_mov_b32_e32 v36, v0
	v_mov_b32_e32 v37, v0
	v_mov_b32_e32 v38, v0
	v_mov_b32_e32 v39, v0
	v_mov_b32_e32 v40, v0
	v_mov_b32_e32 v41, v0
	v_mov_b32_e32 v42, v0
	v_mov_b32_e32 v43, v0
	v_mov_b32_e32 v44, v0
	v_mov_b32_e32 v45, v0
	v_mov_b32_e32 v46, v0
	v_mov_b32_e32 v47, v0
	v_mov_b32_e32 v48, v0
	v_mov_b32_e32 v49, v0
	v_mov_b32_e32 v50, v0
	v_mov_b32_e32 v51, v0
	v_mov_b32_e32 v52, v0
	v_mov_b32_e32 v53, v0
	v_mov_b32_e32 v54, v0
	v_mov_b32_e32 v55, v0
	v_mov_b32_e32 v56, v0
	v_mov_b32_e32 v57, v0
	v_mov_b32_e32 v58, v0
	v_mov_b32_e32 v59, v0
	v_mov_b32_e32 v60, v0
	v_mov_b32_e32 v61, v0
	v_mov_b32_e32 v62, v0
	v_mov_b32_e32 v63, v0
	v_mov_b32_e32 v160, v0
	v_mov_b32_e32 v161, v0
	v_mov_b32_e32 v227, v64
	v_mov_b32_e32 v228, v65
	v_mov_b32_e32 v229, v66
	v_mov_b32_e32 v184, v67
	v_readlane_b32 s100, v250, 8
	v_mbcnt_lo_u32_b32 v68, -1, 0
	v_mbcnt_hi_u32_b32 v68, -1, v68
	v_and_b32_e32 v69, 15, v68
	v_lshrrev_b32_e32 v70, 4, v68
	v_lshlrev_b32_e32 v72, 8, v69
	v_add_u32_e32 v72, 0x10000, v72
	v_add_u32_e32 v71, 0, v70
	v_xor_b32_e32 v71, v71, v69
	v_lshl_add_u32 v201, v71, 4, v72
	v_add_u32_e32 v71, 4, v70
	v_xor_b32_e32 v71, v71, v69
	v_lshl_add_u32 v202, v71, 4, v72
	v_add_u32_e32 v71, 8, v70
	v_xor_b32_e32 v71, v71, v69
	v_lshl_add_u32 v203, v71, 4, v72
	v_add_u32_e32 v71, 12, v70
	v_xor_b32_e32 v71, v71, v69
	v_lshl_add_u32 v246, v71, 4, v72
	v_bfe_u32 v73, v69, 1, 3
	v_lshlrev_b32_e32 v76, 7, v69
	v_add_u32_e32 v71, 0, v70
	v_xor_b32_e32 v71, v71, v73
	v_lshl_add_u32 v209, v71, 4, v76
	v_add_u32_e32 v71, 4, v70
	v_xor_b32_e32 v71, v71, v73
	v_lshl_add_u32 v210, v71, 4, v76
	s_lshl_b32 s101, s100, 7
	s_add_u32 s101, s101, 0x8000
	s_cmpk_ge_u32 s100, 0x100
	s_cselect_b32 s6, 0x8000, 0
	s_add_u32 s101, s101, s6
	v_and_b32_e32 v74, 31, v68
	v_lshrrev_b32_e32 v75, 5, v68
	v_lshlrev_b32_e32 v74, 8, v74
	v_lshl_add_u32 v74, v75, 4, v74
	v_add_u32_e32 v74, s101, v74
	v_lshlrev_b32_e32 v75, 8, v69
	v_lshl_add_u32 v75, v70, 4, v75
	v_add_u32_e32 v75, s101, v75
	ds_write_b128 v74, v[96:99] offset:0
	ds_write_b128 v74, v[100:103] offset:32
	ds_write_b128 v74, v[104:107] offset:64
	ds_write_b128 v74, v[108:111] offset:96
	ds_write_b128 v74, v[112:115] offset:128
	ds_write_b128 v74, v[116:119] offset:160
	ds_write_b128 v74, v[120:123] offset:192
	ds_write_b128 v74, v[124:127] offset:224
	s_waitcnt lgkmcnt(0)
	ds_read_b128 v[96:99], v75 offset:0
	ds_read_b128 v[100:103], v75 offset:64
	ds_read_b128 v[104:107], v75 offset:128
	ds_read_b128 v[108:111], v75 offset:192
	ds_read_b128 v[112:115], v75 offset:4096
	ds_read_b128 v[116:119], v75 offset:4160
	ds_read_b128 v[120:123], v75 offset:4224
	ds_read_b128 v[124:127], v75 offset:4288
	s_waitcnt vmcnt(0)
	s_waitcnt lgkmcnt(0)
	s_barrier
	ds_write_b128 v225, v[136:139] offset:32768
	ds_write_b128 v226, v[140:143] offset:32768
	s_add_u32 s15, s22, s12
	s_addc_u32 s14, s23, s13
	s_add_u32 s6, s15, 0x23a40000
	s_addc_u32 s7, s14, 0
	s_waitcnt lgkmcnt(0)
	global_load_dwordx4 v[136:139], v196, s[6:7]
	global_load_dwordx4 v[140:143], v197, s[6:7]
	v_mov_b32_e32 v194, 0
	v_mov_b32_e32 v195, 0
	s_barrier
	s_cmpk_ge_u32 s100, 0x100
	s_cselect_b32 s100, 1, 0
	ds_read_b128 v[160:163], v201 offset:0
	ds_read_b128 v[164:167], v202 offset:0
	ds_read_b128 v[168:171], v203 offset:0
	ds_read_b128 v[172:175], v246 offset:0
	ds_read_b128 v[176:179], v201 offset:4096
	ds_read_b128 v[180:183], v202 offset:4096
	ds_read_b128 v[230:233], v203 offset:4096
	s_waitcnt lgkmcnt(6)
	v_mfma_f32_16x16x32_bf16 v[64:67], v[160:163], v[96:99], 0
	v_mfma_f32_16x16x32_bf16 v[68:71], v[160:163], v[112:115], 0
	ds_read_b128 v[234:237], v246 offset:4096
	s_waitcnt lgkmcnt(6)
	v_mfma_f32_16x16x32_bf16 v[68:71], v[164:167], v[116:119], v[68:71]
	v_mfma_f32_16x16x32_bf16 v[64:67], v[164:167], v[100:103], v[64:67]
	ds_read_b128 v[160:163], v201 offset:8192
	s_waitcnt lgkmcnt(6)
	v_mfma_f32_16x16x32_bf16 v[64:67], v[168:171], v[104:107], v[64:67]
	v_mfma_f32_16x16x32_bf16 v[68:71], v[168:171], v[120:123], v[68:71]
	ds_read_b128 v[164:167], v202 offset:8192
	s_waitcnt lgkmcnt(6)
	v_mfma_f32_16x16x32_bf16 v[68:71], v[172:175], v[124:127], v[68:71]
	v_mfma_f32_16x16x32_bf16 v[64:67], v[172:175], v[108:111], v[64:67]
	ds_read_b128 v[168:171], v203 offset:8192
	s_waitcnt lgkmcnt(6)
	v_mfma_f32_16x16x32_bf16 v[72:75], v[176:179], v[96:99], 0
	s_nop 7
	s_nop 1
	v_exp_f32_e32 v64, v64
	v_mfma_f32_16x16x32_bf16 v[76:79], v[176:179], v[112:115], 0
	v_exp_f32_e32 v68, v68
	ds_read_b128 v[172:175], v246 offset:8192
	s_waitcnt lgkmcnt(6)
	v_mfma_f32_16x16x32_bf16 v[76:79], v[180:183], v[116:119], v[76:79]
	v_exp_f32_e32 v65, v65
	v_exp_f32_e32 v69, v69
	v_mfma_f32_16x16x32_bf16 v[72:75], v[180:183], v[100:103], v[72:75]
	v_exp_f32_e32 v66, v66
	ds_read_b128 v[176:179], v201 offset:12288
	s_waitcnt lgkmcnt(6)
	v_mfma_f32_16x16x32_bf16 v[72:75], v[230:233], v[104:107], v[72:75]
	v_exp_f32_e32 v70, v70
	v_exp_f32_e32 v67, v67
	v_mfma_f32_16x16x32_bf16 v[76:79], v[230:233], v[120:123], v[76:79]
	v_exp_f32_e32 v71, v71
	v_add_f32_e32 v220, v64, v65
	ds_read_b128 v[180:183], v202 offset:12288
	s_waitcnt lgkmcnt(6)
	v_mfma_f32_16x16x32_bf16 v[76:79], v[234:237], v[124:127], v[76:79]
	v_add_f32_e32 v221, v68, v69
	v_add_f32_e32 v220, v220, v66
	v_add_f32_e32 v221, v221, v70
	v_mfma_f32_16x16x32_bf16 v[72:75], v[234:237], v[108:111], v[72:75]
	v_add_f32_e32 v220, v220, v67
	v_add_f32_e32 v221, v221, v71
	ds_read_b128 v[230:233], v203 offset:12288
	s_waitcnt lgkmcnt(6)
	v_mfma_f32_16x16x32_bf16 v[80:83], v[160:163], v[96:99], 0
	s_nop 7
	s_nop 1
	v_exp_f32_e32 v72, v72
	v_exp_f32_e32 v76, v76
	v_mfma_f32_16x16x32_bf16 v[84:87], v[160:163], v[112:115], 0
	v_exp_f32_e32 v73, v73
	v_exp_f32_e32 v77, v77
	ds_read_b128 v[234:237], v246 offset:12288
	s_waitcnt lgkmcnt(6)
	v_mfma_f32_16x16x32_bf16 v[84:87], v[164:167], v[116:119], v[84:87]
	v_exp_f32_e32 v74, v74
	v_exp_f32_e32 v78, v78
	v_mfma_f32_16x16x32_bf16 v[80:83], v[164:167], v[100:103], v[80:83]
	v_exp_f32_e32 v75, v75
	v_exp_f32_e32 v79, v79
	s_waitcnt lgkmcnt(5)
	v_mfma_f32_16x16x32_bf16 v[80:83], v[168:171], v[104:107], v[80:83]
	v_add_f32_e32 v220, v220, v72
	v_add_f32_e32 v221, v221, v76
	v_add_f32_e32 v220, v220, v73
	v_add_f32_e32 v221, v221, v77
	v_mfma_f32_16x16x32_bf16 v[84:87], v[168:171], v[120:123], v[84:87]
	v_add_f32_e32 v220, v220, v74
	v_add_f32_e32 v221, v221, v78
	v_add_f32_e32 v220, v220, v75
	v_add_f32_e32 v221, v221, v79
	s_waitcnt lgkmcnt(4)
	v_mfma_f32_16x16x32_bf16 v[84:87], v[172:175], v[124:127], v[84:87]
	v_cvt_pk_bf16_f32 v216, v64, v65
	v_cvt_pk_bf16_f32 v217, v66, v67
	v_cvt_pk_bf16_f32 v238, v68, v69
	v_cvt_pk_bf16_f32 v239, v70, v71
	v_mfma_f32_16x16x32_bf16 v[80:83], v[172:175], v[108:111], v[80:83]
	v_cvt_pk_bf16_f32 v218, v72, v73
	v_cvt_pk_bf16_f32 v219, v74, v75
	v_cvt_pk_bf16_f32 v240, v76, v77
	v_cvt_pk_bf16_f32 v241, v78, v79
	s_waitcnt lgkmcnt(3)
	v_mfma_f32_16x16x32_bf16 v[88:91], v[176:179], v[96:99], 0
	s_nop 7
	s_nop 1
	v_exp_f32_e32 v80, v80
	v_exp_f32_e32 v84, v84
	v_mfma_f32_16x16x32_bf16 v[92:95], v[176:179], v[112:115], 0
	v_exp_f32_e32 v81, v81
	s_waitcnt lgkmcnt(2)
	v_mfma_f32_16x16x32_bf16 v[92:95], v[180:183], v[116:119], v[92:95]
	v_exp_f32_e32 v85, v85
	v_exp_f32_e32 v82, v82
	v_mfma_f32_16x16x32_bf16 v[88:91], v[180:183], v[100:103], v[88:91]
	v_exp_f32_e32 v86, v86
	s_waitcnt lgkmcnt(1)
	v_mfma_f32_16x16x32_bf16 v[88:91], v[230:233], v[104:107], v[88:91]
	v_exp_f32_e32 v83, v83
	v_exp_f32_e32 v87, v87
	v_mfma_f32_16x16x32_bf16 v[92:95], v[230:233], v[120:123], v[92:95]
	v_add_f32_e32 v220, v220, v80
	v_add_f32_e32 v221, v221, v84
	v_add_f32_e32 v220, v220, v81
	s_waitcnt lgkmcnt(0)
	v_mfma_f32_16x16x32_bf16 v[92:95], v[234:237], v[124:127], v[92:95]
	v_add_f32_e32 v221, v221, v85
	v_add_f32_e32 v220, v220, v82
	v_add_f32_e32 v221, v221, v86
	v_mfma_f32_16x16x32_bf16 v[88:91], v[234:237], v[108:111], v[88:91]
	v_add_f32_e32 v220, v220, v83
	v_add_f32_e32 v221, v221, v87
	s_waitcnt lgkmcnt(0)
	s_barrier
	ds_read_b128 v[160:163], v201 offset:16384
	ds_read_b128 v[164:167], v209 offset:0
	ds_read_b128 v[168:171], v202 offset:16384
	ds_read_b128 v[172:175], v209 offset:2048
	ds_read_b128 v[176:179], v203 offset:16384
	ds_read_b128 v[180:183], v209 offset:4096
	ds_read_b128 v[230:233], v246 offset:16384
	.p2align 6

.Lattn_pb0:
	s_waitcnt lgkmcnt(6)
	v_mfma_f32_16x16x32_bf16 v[64:67], v[160:163], v[96:99], 0
	v_exp_f32_e32 v88, v88
	v_mfma_f32_16x16x32_bf16 v[68:71], v[160:163], v[112:115], 0
	v_exp_f32_e32 v92, v92
	ds_read_b128 v[234:237], v209 offset:6144
	s_add_u32 s16, s22, s10
	s_addc_u32 s17, s23, s11
	s_add_u32 s15, s22, s12
	s_addc_u32 s14, s23, s13
	s_add_u32 s8, s16, 0x3bc00200
	s_addc_u32 s9, s17, 0
	s_add_u32 s6, s15, 0x23a50000
	s_addc_u32 s7, s14, 0
	s_waitcnt lgkmcnt(6)
	v_mfma_f32_16x16x32_bf16 v[0:3], v[164:167], v[216:219], v[0:3]
	v_cvt_pk_bf16_f32 v242, v80, v81
	v_mfma_f32_16x16x32_bf16 v[4:7], v[164:167], v[238:241], v[4:7]
	v_exp_f32_e32 v89, v89
	ds_read_b128 v[160:163], v201 offset:20480
	s_waitcnt vmcnt(4)
	ds_write_b128 v225, v[152:155] offset:49152
	s_waitcnt lgkmcnt(7)
	v_mfma_f32_16x16x32_bf16 v[68:71], v[168:171], v[116:119], v[68:71]
	v_exp_f32_e64 v93, v93
	v_mfma_f32_16x16x32_bf16 v[64:67], v[168:171], v[100:103], v[64:67]
	v_cvt_pk_bf16_f32 v243, v82, v83
	ds_read_b128 v[164:167], v209 offset:8192
	ds_write_b128 v226, v[156:159] offset:49152
	s_waitcnt lgkmcnt(8)
	v_mfma_f32_16x16x32_bf16 v[12:15], v[172:175], v[238:241], v[12:15]
	v_exp_f32_e32 v90, v90
	v_mfma_f32_16x16x32_bf16 v[8:11], v[172:175], v[216:219], v[8:11]
	v_exp_f32_e32 v94, v94
	ds_read_b128 v[168:171], v202 offset:20480
	ds_write_b64 v227, v[132:133] offset:32768
	s_waitcnt lgkmcnt(9)
	v_mfma_f32_16x16x32_bf16 v[64:67], v[176:179], v[104:107], v[64:67]
	v_cvt_pk_bf16_f32 v204, v84, v85
	v_mfma_f32_16x16x32_bf16 v[68:71], v[176:179], v[120:123], v[68:71]
	v_exp_f32_e64 v91, v91
	ds_read_b128 v[172:175], v209 offset:10240
	ds_write_b64 v228, v[134:135] offset:32768
	s_waitcnt lgkmcnt(10)
	v_mfma_f32_16x16x32_bf16 v[16:19], v[180:183], v[216:219], v[16:19]
	v_exp_f32_e32 v95, v95
	v_mfma_f32_16x16x32_bf16 v[20:23], v[180:183], v[238:241], v[20:23]
	v_cvt_pk_bf16_f32 v205, v86, v87
	v_add_f32_e32 v220, v220, v88
	ds_read_b128 v[176:179], v203 offset:20480
	ds_write_b64 v229, v[128:129] offset:32768
	s_waitcnt lgkmcnt(11)
	v_mfma_f32_16x16x32_bf16 v[68:71], v[230:233], v[124:127], v[68:71]
	v_add_f32_e32 v221, v221, v92
	v_add_f32_e32 v220, v220, v89
	v_mfma_f32_16x16x32_bf16 v[64:67], v[230:233], v[108:111], v[64:67]
	v_add_f32_e64 v221, v221, v93
	v_cvt_pk_bf16_f32 v244, v88, v89
	ds_read_b128 v[180:183], v209 offset:12288
	ds_write_b64 v184, v[130:131] offset:32768
	s_waitcnt lgkmcnt(12)
	s_nop 0
	v_mfma_f32_16x16x32_bf16 v[28:31], v[234:237], v[238:241], v[28:31]
	v_cvt_pk_bf16_f32 v245, v90, v91
	v_cvt_pk_bf16_f32 v206, v92, v93
	v_mfma_f32_16x16x32_bf16 v[24:27], v[234:237], v[216:219], v[24:27]
	v_cvt_pk_bf16_f32 v207, v94, v95
	ds_read_b128 v[230:233], v246 offset:20480
	global_load_dwordx4 v[132:135], v198, s[8:9]
	s_waitcnt lgkmcnt(12)
	s_nop 0
	v_mfma_f32_16x16x32_bf16 v[72:75], v[160:163], v[96:99], 0
	v_add_f32_e32 v220, v220, v90
	v_add_f32_e32 v221, v221, v94
	v_mfma_f32_16x16x32_bf16 v[76:79], v[160:163], v[112:115], 0
	v_add_f32_e32 v220, v220, v91
	v_add_f32_e32 v221, v221, v95
	ds_read_b128 v[234:237], v209 offset:14336
	global_load_dwordx4 v[128:131], v199, s[8:9]
	s_waitcnt lgkmcnt(11)
	v_mfma_f32_16x16x32_bf16 v[32:35], v[164:167], v[216:219], v[32:35]
	v_add_f32_e32 v194, v194, v220
	v_add_f32_e32 v195, v195, v221
	v_mfma_f32_16x16x32_bf16 v[36:39], v[164:167], v[238:241], v[36:39]
	v_exp_f32_e32 v64, v64
	ds_read_b128 v[160:163], v201 offset:24576
	global_load_dwordx4 v[152:155], v196, s[6:7]
	s_waitcnt lgkmcnt(10)
	v_mfma_f32_16x16x32_bf16 v[76:79], v[168:171], v[116:119], v[76:79]
	v_exp_f32_e32 v68, v68
	v_mfma_f32_16x16x32_bf16 v[72:75], v[168:171], v[100:103], v[72:75]
	v_exp_f32_e64 v65, v65
	ds_read_b128 v[164:167], v210 offset:0
	global_load_dwordx4 v[156:159], v197, s[6:7]
	s_waitcnt lgkmcnt(9)
	v_mfma_f32_16x16x32_bf16 v[44:47], v[172:175], v[238:241], v[44:47]
	v_exp_f32_e32 v69, v69
	v_mfma_f32_16x16x32_bf16 v[40:43], v[172:175], v[216:219], v[40:43]
	v_exp_f32_e32 v66, v66
	ds_read_b128 v[168:171], v202 offset:24576
	s_waitcnt lgkmcnt(8)
	v_mfma_f32_16x16x32_bf16 v[72:75], v[176:179], v[104:107], v[72:75]
	v_exp_f32_e32 v70, v70
	v_mfma_f32_16x16x32_bf16 v[76:79], v[176:179], v[120:123], v[76:79]
	v_exp_f32_e64 v67, v67
	ds_read_b128 v[172:175], v210 offset:2048
	s_waitcnt lgkmcnt(7)
	v_mfma_f32_16x16x32_bf16 v[48:51], v[180:183], v[216:219], v[48:51]
	v_exp_f32_e32 v71, v71
	v_mfma_f32_16x16x32_bf16 v[52:55], v[180:183], v[238:241], v[52:55]
	v_add_f32_e32 v220, v64, v65
	ds_read_b128 v[176:179], v203 offset:24576
	s_waitcnt lgkmcnt(6)
	v_mfma_f32_16x16x32_bf16 v[76:79], v[230:233], v[124:127], v[76:79]
	v_add_f32_e32 v221, v68, v69
	v_mfma_f32_16x16x32_bf16 v[72:75], v[230:233], v[108:111], v[72:75]
	v_add_f32_e64 v220, v220, v66
	ds_read_b128 v[180:183], v210 offset:4096
	s_waitcnt lgkmcnt(6)
	v_mfma_f32_16x16x32_bf16 v[60:63], v[234:237], v[238:241], v[60:63]
	v_add_f32_e32 v221, v221, v70
	v_add_f32_e64 v220, v220, v67
	v_mfma_f32_16x16x32_bf16 v[56:59], v[234:237], v[216:219], v[56:59]
	v_add_f32_e32 v221, v221, v71
	ds_read_b128 v[230:233], v246 offset:24576
	s_waitcnt lgkmcnt(6)
	v_mfma_f32_16x16x32_bf16 v[80:83], v[160:163], v[96:99], 0
	v_exp_f32_e32 v72, v72
	v_mfma_f32_16x16x32_bf16 v[84:87], v[160:163], v[112:115], 0
	v_exp_f32_e64 v76, v76
	ds_read_b128 v[234:237], v210 offset:6144
	s_waitcnt lgkmcnt(6)
	v_mfma_f32_16x16x32_bf16 v[0:3], v[164:167], v[242:245], v[0:3]
	v_exp_f32_e32 v73, v73
	v_mfma_f32_16x16x32_bf16 v[4:7], v[164:167], v[204:207], v[4:7]
	v_exp_f32_e32 v77, v77
	ds_read_b128 v[160:163], v201 offset:28672
	s_waitcnt lgkmcnt(6)
	v_mfma_f32_16x16x32_bf16 v[84:87], v[168:171], v[116:119], v[84:87]
	v_exp_f32_e32 v74, v74
	v_mfma_f32_16x16x32_bf16 v[80:83], v[168:171], v[100:103], v[80:83]
	v_exp_f32_e64 v78, v78
	ds_read_b128 v[164:167], v210 offset:8192
	s_waitcnt lgkmcnt(6)
	v_mfma_f32_16x16x32_bf16 v[12:15], v[172:175], v[204:207], v[12:15]
	v_exp_f32_e32 v75, v75
	v_mfma_f32_16x16x32_bf16 v[8:11], v[172:175], v[242:245], v[8:11]
	v_exp_f32_e32 v79, v79
	ds_read_b128 v[168:171], v202 offset:28672
	s_waitcnt lgkmcnt(6)
	v_mfma_f32_16x16x32_bf16 v[80:83], v[176:179], v[104:107], v[80:83]
	v_add_f32_e32 v220, v220, v72
	v_add_f32_e32 v221, v221, v76
	v_mfma_f32_16x16x32_bf16 v[84:87], v[176:179], v[120:123], v[84:87]
	v_add_f32_e32 v220, v220, v73
	ds_read_b128 v[172:175], v210 offset:10240
	s_waitcnt lgkmcnt(6)
	v_mfma_f32_16x16x32_bf16 v[16:19], v[180:183], v[242:245], v[16:19]
	v_add_f32_e32 v221, v221, v77
	v_add_f32_e32 v220, v220, v74
	v_mfma_f32_16x16x32_bf16 v[20:23], v[180:183], v[204:207], v[20:23]
	v_add_f32_e32 v221, v221, v78
	ds_read_b128 v[176:179], v203 offset:28672
	s_waitcnt lgkmcnt(6)
	v_mfma_f32_16x16x32_bf16 v[84:87], v[230:233], v[124:127], v[84:87]
	v_add_f32_e32 v220, v220, v75
	v_add_f32_e32 v221, v221, v79
	v_mfma_f32_16x16x32_bf16 v[80:83], v[230:233], v[108:111], v[80:83]
	v_cvt_pk_bf16_f32 v216, v64, v65
	ds_read_b128 v[180:183], v210 offset:12288
	s_waitcnt lgkmcnt(6)
	v_mfma_f32_16x16x32_bf16 v[28:31], v[234:237], v[204:207], v[28:31]
	v_cvt_pk_bf16_f32 v217, v66, v67
	s_nop 0
	v_cvt_pk_bf16_f32 v238, v68, v69
	v_mfma_f32_16x16x32_bf16 v[24:27], v[234:237], v[242:245], v[24:27]
	v_cvt_pk_bf16_f32 v239, v70, v71
	ds_read_b128 v[230:233], v246 offset:28672
	s_waitcnt lgkmcnt(6)
	v_mfma_f32_16x16x32_bf16 v[88:91], v[160:163], v[96:99], 0
	v_exp_f32_e32 v80, v80
	v_mfma_f32_16x16x32_bf16 v[92:95], v[160:163], v[112:115], 0
	v_exp_f32_e64 v84, v84
	ds_read_b128 v[234:237], v210 offset:14336
	s_waitcnt lgkmcnt(6)
	v_mfma_f32_16x16x32_bf16 v[32:35], v[164:167], v[242:245], v[32:35]
	v_exp_f32_e32 v81, v81
	v_mfma_f32_16x16x32_bf16 v[36:39], v[164:167], v[204:207], v[36:39]
	v_exp_f32_e32 v85, v85
	ds_read_b128 v[160:163], v201 offset:32768
	s_waitcnt lgkmcnt(6)
	v_mfma_f32_16x16x32_bf16 v[92:95], v[168:171], v[116:119], v[92:95]
	v_exp_f32_e64 v82, v82
	v_mfma_f32_16x16x32_bf16 v[88:91], v[168:171], v[100:103], v[88:91]
	v_exp_f32_e32 v86, v86
	ds_read_b128 v[164:167], v209 offset:16384
	s_waitcnt lgkmcnt(6)
	v_mfma_f32_16x16x32_bf16 v[44:47], v[172:175], v[204:207], v[44:47]
	v_exp_f32_e32 v83, v83
	v_mfma_f32_16x16x32_bf16 v[40:43], v[172:175], v[242:245], v[40:43]
	v_exp_f32_e64 v87, v87
	ds_read_b128 v[168:171], v202 offset:32768
	s_waitcnt lgkmcnt(6)
	v_mfma_f32_16x16x32_bf16 v[88:91], v[176:179], v[104:107], v[88:91]
	v_add_f32_e32 v220, v220, v80
	v_add_f32_e32 v221, v221, v84
	v_mfma_f32_16x16x32_bf16 v[92:95], v[176:179], v[120:123], v[92:95]
	v_add_f32_e64 v220, v220, v81
	ds_read_b128 v[172:175], v209 offset:18432
	s_waitcnt lgkmcnt(6)
	v_mfma_f32_16x16x32_bf16 v[48:51], v[180:183], v[242:245], v[48:51]
	v_add_f32_e32 v221, v221, v85
	v_add_f32_e64 v220, v220, v82
	v_mfma_f32_16x16x32_bf16 v[52:55], v[180:183], v[204:207], v[52:55]
	v_add_f32_e32 v221, v221, v86
	ds_read_b128 v[176:179], v203 offset:32768
	s_waitcnt lgkmcnt(6)
	v_mfma_f32_16x16x32_bf16 v[92:95], v[230:233], v[124:127], v[92:95]
	v_add_f32_e32 v220, v220, v83
	v_add_f32_e32 v221, v221, v87
	v_mfma_f32_16x16x32_bf16 v[88:91], v[230:233], v[108:111], v[88:91]
	v_cvt_pk_bf16_f32 v218, v72, v73
	ds_read_b128 v[180:183], v209 offset:20480
	s_waitcnt lgkmcnt(6)
	v_mfma_f32_16x16x32_bf16 v[60:63], v[234:237], v[204:207], v[60:63]
	v_cvt_pk_bf16_f32 v219, v74, v75
	v_cvt_pk_bf16_f32 v240, v76, v77
	s_nop 0
	v_mfma_f32_16x16x32_bf16 v[56:59], v[234:237], v[242:245], v[56:59]
	v_cvt_pk_bf16_f32 v241, v78, v79
	ds_read_b128 v[230:233], v246 offset:32768
	s_cmp_eq_u32 s100, 1
	s_cbranch_scc1 .Lattn_pa1
	s_setprio 1
	s_branch .Lattn_pb1

.Lattn_pb1:
	s_waitcnt lgkmcnt(6)
	v_mfma_f32_16x16x32_bf16 v[64:67], v[160:163], v[96:99], 0
	v_exp_f32_e64 v88, v88
	v_mfma_f32_16x16x32_bf16 v[68:71], v[160:163], v[112:115], 0
	v_exp_f32_e32 v92, v92
	ds_read_b128 v[234:237], v209 offset:22528
	s_add_u32 s8, s16, 0x3bc00280
	s_addc_u32 s9, s17, 0
	s_add_u32 s6, s15, 0x23a60000
	s_addc_u32 s7, s14, 0
	s_waitcnt lgkmcnt(6)
	v_mfma_f32_16x16x32_bf16 v[0:3], v[164:167], v[216:219], v[0:3]
	v_cvt_pk_bf16_f32 v242, v80, v81
	v_mfma_f32_16x16x32_bf16 v[4:7], v[164:167], v[238:241], v[4:7]
	v_exp_f32_e32 v89, v89
	ds_read_b128 v[160:163], v201 offset:36864
	s_waitcnt vmcnt(4)
	ds_write_b128 v225, v[136:139] offset:0
	s_waitcnt lgkmcnt(7)
	v_mfma_f32_16x16x32_bf16 v[68:71], v[168:171], v[116:119], v[68:71]
	v_exp_f32_e32 v93, v93
	v_mfma_f32_16x16x32_bf16 v[64:67], v[168:171], v[100:103], v[64:67]
	v_cvt_pk_bf16_f32 v243, v82, v83
	ds_read_b128 v[164:167], v209 offset:24576
	ds_write_b128 v226, v[140:143] offset:0
	s_waitcnt lgkmcnt(8)
	v_mfma_f32_16x16x32_bf16 v[12:15], v[172:175], v[238:241], v[12:15]
	v_exp_f32_e32 v90, v90
	v_mfma_f32_16x16x32_bf16 v[8:11], v[172:175], v[216:219], v[8:11]
	v_exp_f32_e32 v94, v94
	ds_read_b128 v[168:171], v202 offset:36864
	ds_write_b64 v227, v[148:149] offset:49152
	s_waitcnt lgkmcnt(9)
	v_mfma_f32_16x16x32_bf16 v[64:67], v[176:179], v[104:107], v[64:67]
	v_cvt_pk_bf16_f32 v204, v84, v85
	v_mfma_f32_16x16x32_bf16 v[68:71], v[176:179], v[120:123], v[68:71]
	v_exp_f32_e64 v91, v91
	ds_read_b128 v[172:175], v209 offset:26624
	ds_write_b64 v228, v[150:151] offset:49152
	s_waitcnt lgkmcnt(10)
	v_mfma_f32_16x16x32_bf16 v[16:19], v[180:183], v[216:219], v[16:19]
	v_exp_f32_e32 v95, v95
	v_mfma_f32_16x16x32_bf16 v[20:23], v[180:183], v[238:241], v[20:23]
	v_cvt_pk_bf16_f32 v205, v86, v87
	v_add_f32_e64 v220, v220, v88
	ds_read_b128 v[176:179], v203 offset:36864
	ds_write_b64 v229, v[144:145] offset:49152
	s_waitcnt lgkmcnt(11)
	v_mfma_f32_16x16x32_bf16 v[68:71], v[230:233], v[124:127], v[68:71]
	v_add_f32_e32 v221, v221, v92
	v_add_f32_e64 v220, v220, v89
	v_mfma_f32_16x16x32_bf16 v[64:67], v[230:233], v[108:111], v[64:67]
	v_add_f32_e64 v221, v221, v93
	v_cvt_pk_bf16_f32 v244, v88, v89
	ds_read_b128 v[180:183], v209 offset:28672
	ds_write_b64 v184, v[146:147] offset:49152
	s_waitcnt lgkmcnt(12)
	v_mfma_f32_16x16x32_bf16 v[28:31], v[234:237], v[238:241], v[28:31]
	v_cvt_pk_bf16_f32 v245, v90, v91
	s_nop 0
	v_cvt_pk_bf16_f32 v206, v92, v93
	v_mfma_f32_16x16x32_bf16 v[24:27], v[234:237], v[216:219], v[24:27]
	v_cvt_pk_bf16_f32 v207, v94, v95
	ds_read_b128 v[230:233], v246 offset:36864
	global_load_dwordx4 v[148:151], v198, s[8:9]
	s_waitcnt lgkmcnt(12)
	v_mfma_f32_16x16x32_bf16 v[72:75], v[160:163], v[96:99], 0
	v_add_f32_e32 v220, v220, v90
	v_add_f32_e64 v221, v221, v94
	v_mfma_f32_16x16x32_bf16 v[76:79], v[160:163], v[112:115], 0
	v_add_f32_e32 v220, v220, v91
	v_add_f32_e32 v221, v221, v95
	ds_read_b128 v[234:237], v209 offset:30720
	global_load_dwordx4 v[144:147], v199, s[8:9]
	s_waitcnt lgkmcnt(11)
	v_mfma_f32_16x16x32_bf16 v[32:35], v[164:167], v[216:219], v[32:35]
	v_add_f32_e32 v194, v194, v220
	v_add_f32_e32 v195, v195, v221
	v_mfma_f32_16x16x32_bf16 v[36:39], v[164:167], v[238:241], v[36:39]
	v_exp_f32_e32 v64, v64
	ds_read_b128 v[160:163], v201 offset:40960
	global_load_dwordx4 v[136:139], v196, s[6:7]
	s_waitcnt lgkmcnt(10)
	v_mfma_f32_16x16x32_bf16 v[76:79], v[168:171], v[116:119], v[76:79]
	v_exp_f32_e32 v68, v68
	v_mfma_f32_16x16x32_bf16 v[72:75], v[168:171], v[100:103], v[72:75]
	v_exp_f32_e32 v65, v65
	ds_read_b128 v[164:167], v210 offset:16384
	global_load_dwordx4 v[140:143], v197, s[6:7]
	s_waitcnt lgkmcnt(9)
	v_mfma_f32_16x16x32_bf16 v[44:47], v[172:175], v[238:241], v[44:47]
	v_exp_f32_e32 v69, v69
	v_mfma_f32_16x16x32_bf16 v[40:43], v[172:175], v[216:219], v[40:43]
	v_exp_f32_e32 v66, v66
	ds_read_b128 v[168:171], v202 offset:40960
	s_waitcnt lgkmcnt(8)
	v_mfma_f32_16x16x32_bf16 v[72:75], v[176:179], v[104:107], v[72:75]
	v_exp_f32_e32 v70, v70
	v_mfma_f32_16x16x32_bf16 v[76:79], v[176:179], v[120:123], v[76:79]
	v_exp_f32_e64 v67, v67
	ds_read_b128 v[172:175], v210 offset:18432
	s_waitcnt lgkmcnt(7)
	v_mfma_f32_16x16x32_bf16 v[48:51], v[180:183], v[216:219], v[48:51]
	v_exp_f32_e32 v71, v71
	v_mfma_f32_16x16x32_bf16 v[52:55], v[180:183], v[238:241], v[52:55]
	v_add_f32_e32 v220, v64, v65
	ds_read_b128 v[176:179], v203 offset:40960
	s_waitcnt lgkmcnt(6)
	v_mfma_f32_16x16x32_bf16 v[76:79], v[230:233], v[124:127], v[76:79]
	v_add_f32_e64 v221, v68, v69
	v_mfma_f32_16x16x32_bf16 v[72:75], v[230:233], v[108:111], v[72:75]
	v_add_f32_e32 v220, v220, v66
	ds_read_b128 v[180:183], v210 offset:20480
	s_waitcnt lgkmcnt(6)
	v_mfma_f32_16x16x32_bf16 v[60:63], v[234:237], v[238:241], v[60:63]
	v_add_f32_e32 v221, v221, v70
	v_add_f32_e32 v220, v220, v67
	v_mfma_f32_16x16x32_bf16 v[56:59], v[234:237], v[216:219], v[56:59]
	v_add_f32_e32 v221, v221, v71
	ds_read_b128 v[230:233], v246 offset:40960
	s_waitcnt lgkmcnt(6)
	v_mfma_f32_16x16x32_bf16 v[80:83], v[160:163], v[96:99], 0
	v_exp_f32_e32 v72, v72
	v_mfma_f32_16x16x32_bf16 v[84:87], v[160:163], v[112:115], 0
	v_exp_f32_e32 v76, v76
	ds_read_b128 v[234:237], v210 offset:22528
	s_waitcnt lgkmcnt(6)
	v_mfma_f32_16x16x32_bf16 v[0:3], v[164:167], v[242:245], v[0:3]
	v_exp_f32_e32 v73, v73
	v_mfma_f32_16x16x32_bf16 v[4:7], v[164:167], v[204:207], v[4:7]
	v_exp_f32_e64 v77, v77
	ds_read_b128 v[160:163], v201 offset:45056
	s_waitcnt lgkmcnt(6)
	v_mfma_f32_16x16x32_bf16 v[84:87], v[168:171], v[116:119], v[84:87]
	v_exp_f32_e32 v74, v74
	v_mfma_f32_16x16x32_bf16 v[80:83], v[168:171], v[100:103], v[80:83]
	v_exp_f32_e32 v78, v78
	ds_read_b128 v[164:167], v210 offset:24576
	s_waitcnt lgkmcnt(6)
	v_mfma_f32_16x16x32_bf16 v[12:15], v[172:175], v[204:207], v[12:15]
	v_exp_f32_e64 v75, v75
	v_mfma_f32_16x16x32_bf16 v[8:11], v[172:175], v[242:245], v[8:11]
	v_exp_f32_e32 v79, v79
	ds_read_b128 v[168:171], v202 offset:45056
	s_waitcnt lgkmcnt(6)
	v_mfma_f32_16x16x32_bf16 v[80:83], v[176:179], v[104:107], v[80:83]
	v_add_f32_e32 v220, v220, v72
	v_add_f32_e32 v221, v221, v76
	v_mfma_f32_16x16x32_bf16 v[84:87], v[176:179], v[120:123], v[84:87]
	v_add_f32_e32 v220, v220, v73
	ds_read_b128 v[172:175], v210 offset:26624
	s_waitcnt lgkmcnt(6)
	v_mfma_f32_16x16x32_bf16 v[16:19], v[180:183], v[242:245], v[16:19]
	v_add_f32_e32 v221, v221, v77
	v_add_f32_e32 v220, v220, v74
	v_mfma_f32_16x16x32_bf16 v[20:23], v[180:183], v[204:207], v[20:23]
	v_add_f32_e64 v221, v221, v78
	ds_read_b128 v[176:179], v203 offset:45056
	s_waitcnt lgkmcnt(6)
	v_mfma_f32_16x16x32_bf16 v[84:87], v[230:233], v[124:127], v[84:87]
	v_add_f32_e32 v220, v220, v75
	v_add_f32_e64 v221, v221, v79
	v_mfma_f32_16x16x32_bf16 v[80:83], v[230:233], v[108:111], v[80:83]
	v_cvt_pk_bf16_f32 v216, v64, v65
	ds_read_b128 v[180:183], v210 offset:28672
	s_waitcnt lgkmcnt(6)
	s_nop 0
	v_mfma_f32_16x16x32_bf16 v[28:31], v[234:237], v[204:207], v[28:31]
	v_cvt_pk_bf16_f32 v217, v66, v67
	v_cvt_pk_bf16_f32 v238, v68, v69
	v_mfma_f32_16x16x32_bf16 v[24:27], v[234:237], v[242:245], v[24:27]
	v_cvt_pk_bf16_f32 v239, v70, v71
	ds_read_b128 v[230:233], v246 offset:45056
	s_waitcnt lgkmcnt(6)
	v_mfma_f32_16x16x32_bf16 v[88:91], v[160:163], v[96:99], 0
	v_exp_f32_e32 v80, v80
	v_mfma_f32_16x16x32_bf16 v[92:95], v[160:163], v[112:115], 0
	v_exp_f32_e32 v84, v84
	ds_read_b128 v[234:237], v210 offset:30720
	s_waitcnt lgkmcnt(6)
	v_mfma_f32_16x16x32_bf16 v[32:35], v[164:167], v[242:245], v[32:35]
	v_exp_f32_e32 v81, v81
	v_mfma_f32_16x16x32_bf16 v[36:39], v[164:167], v[204:207], v[36:39]
	v_exp_f32_e32 v85, v85
	s_waitcnt lgkmcnt(5)
	v_mfma_f32_16x16x32_bf16 v[92:95], v[168:171], v[116:119], v[92:95]
	v_exp_f32_e32 v82, v82
	v_mfma_f32_16x16x32_bf16 v[88:91], v[168:171], v[100:103], v[88:91]
	v_exp_f32_e32 v86, v86
	s_waitcnt lgkmcnt(4)
	v_mfma_f32_16x16x32_bf16 v[44:47], v[172:175], v[204:207], v[44:47]
	v_exp_f32_e64 v83, v83
	v_mfma_f32_16x16x32_bf16 v[40:43], v[172:175], v[242:245], v[40:43]
	v_exp_f32_e32 v87, v87
	s_waitcnt lgkmcnt(3)
	v_mfma_f32_16x16x32_bf16 v[88:91], v[176:179], v[104:107], v[88:91]
	v_add_f32_e32 v220, v220, v80
	v_add_f32_e32 v221, v221, v84
	v_mfma_f32_16x16x32_bf16 v[92:95], v[176:179], v[120:123], v[92:95]
	v_add_f32_e64 v220, v220, v81
	s_waitcnt lgkmcnt(0)
	s_barrier
	ds_read_b128 v[160:163], v201 offset:49152
	ds_read_b128 v[164:167], v209 offset:32768
	ds_read_b128 v[168:171], v202 offset:49152
	ds_read_b128 v[172:175], v209 offset:34816
	v_mfma_f32_16x16x32_bf16 v[48:51], v[180:183], v[242:245], v[48:51]
	v_add_f32_e32 v221, v221, v85
	v_add_f32_e32 v220, v220, v82
	v_mfma_f32_16x16x32_bf16 v[52:55], v[180:183], v[204:207], v[52:55]
	v_add_f32_e64 v221, v221, v86
	ds_read_b128 v[176:179], v203 offset:49152
	v_mfma_f32_16x16x32_bf16 v[92:95], v[230:233], v[124:127], v[92:95]
	v_add_f32_e32 v220, v220, v83
	v_add_f32_e32 v221, v221, v87
	v_mfma_f32_16x16x32_bf16 v[88:91], v[230:233], v[108:111], v[88:91]
	v_cvt_pk_bf16_f32 v218, v72, v73
	ds_read_b128 v[180:183], v209 offset:36864
	v_mfma_f32_16x16x32_bf16 v[60:63], v[234:237], v[204:207], v[60:63]
	v_cvt_pk_bf16_f32 v219, v74, v75
	v_cvt_pk_bf16_f32 v240, v76, v77
	v_mfma_f32_16x16x32_bf16 v[56:59], v[234:237], v[242:245], v[56:59]
	v_cvt_pk_bf16_f32 v241, v78, v79
	ds_read_b128 v[230:233], v246 offset:49152
	s_cmp_eq_u32 s100, 0
	s_cbranch_scc1 .Lattn_pa2
	s_setprio 1
	s_branch .Lattn_pb2

.Lattn_pb2:
	s_waitcnt lgkmcnt(6)
	v_mfma_f32_16x16x32_bf16 v[64:67], v[160:163], v[96:99], 0
	v_exp_f32_e64 v88, v88
	v_mfma_f32_16x16x32_bf16 v[68:71], v[160:163], v[112:115], 0
	v_exp_f32_e32 v92, v92
	ds_read_b128 v[234:237], v209 offset:38912
	s_add_u32 s8, s16, 0x3bc00300
	s_addc_u32 s9, s17, 0
	s_add_u32 s6, s15, 0x23a70000
	s_addc_u32 s7, s14, 0
	s_waitcnt lgkmcnt(6)
	v_mfma_f32_16x16x32_bf16 v[0:3], v[164:167], v[216:219], v[0:3]
	v_cvt_pk_bf16_f32 v242, v80, v81
	v_mfma_f32_16x16x32_bf16 v[4:7], v[164:167], v[238:241], v[4:7]
	v_exp_f32_e32 v89, v89
	ds_read_b128 v[160:163], v201 offset:53248
	s_waitcnt vmcnt(4)
	ds_write_b128 v225, v[152:155] offset:16384
	s_waitcnt lgkmcnt(7)
	v_mfma_f32_16x16x32_bf16 v[68:71], v[168:171], v[116:119], v[68:71]
	v_exp_f32_e32 v93, v93
	v_mfma_f32_16x16x32_bf16 v[64:67], v[168:171], v[100:103], v[64:67]
	v_cvt_pk_bf16_f32 v243, v82, v83
	ds_read_b128 v[164:167], v209 offset:40960
	ds_write_b128 v226, v[156:159] offset:16384
	s_waitcnt lgkmcnt(8)
	v_mfma_f32_16x16x32_bf16 v[12:15], v[172:175], v[238:241], v[12:15]
	v_exp_f32_e32 v90, v90
	v_mfma_f32_16x16x32_bf16 v[8:11], v[172:175], v[216:219], v[8:11]
	v_exp_f32_e32 v94, v94
	ds_read_b128 v[168:171], v202 offset:53248
	ds_write_b64 v227, v[132:133] offset:0
	s_waitcnt lgkmcnt(9)
	v_mfma_f32_16x16x32_bf16 v[64:67], v[176:179], v[104:107], v[64:67]
	v_cvt_pk_bf16_f32 v204, v84, v85
	v_mfma_f32_16x16x32_bf16 v[68:71], v[176:179], v[120:123], v[68:71]
	v_exp_f32_e64 v91, v91
	ds_read_b128 v[172:175], v209 offset:43008
	ds_write_b64 v228, v[134:135] offset:0
	s_waitcnt lgkmcnt(10)
	v_mfma_f32_16x16x32_bf16 v[16:19], v[180:183], v[216:219], v[16:19]
	v_exp_f32_e32 v95, v95
	v_mfma_f32_16x16x32_bf16 v[20:23], v[180:183], v[238:241], v[20:23]
	v_cvt_pk_bf16_f32 v205, v86, v87
	v_add_f32_e64 v220, v220, v88
	ds_read_b128 v[176:179], v203 offset:53248
	ds_write_b64 v229, v[128:129] offset:0
	s_waitcnt lgkmcnt(11)
	v_mfma_f32_16x16x32_bf16 v[68:71], v[230:233], v[124:127], v[68:71]
	v_add_f32_e32 v221, v221, v92
	v_add_f32_e64 v220, v220, v89
	v_mfma_f32_16x16x32_bf16 v[64:67], v[230:233], v[108:111], v[64:67]
	v_add_f32_e64 v221, v221, v93
	v_cvt_pk_bf16_f32 v244, v88, v89
	ds_read_b128 v[180:183], v209 offset:45056
	ds_write_b64 v184, v[130:131] offset:0
	s_waitcnt lgkmcnt(12)
	v_mfma_f32_16x16x32_bf16 v[28:31], v[234:237], v[238:241], v[28:31]
	v_cvt_pk_bf16_f32 v245, v90, v91
	s_nop 0
	v_cvt_pk_bf16_f32 v206, v92, v93
	v_mfma_f32_16x16x32_bf16 v[24:27], v[234:237], v[216:219], v[24:27]
	v_cvt_pk_bf16_f32 v207, v94, v95
	ds_read_b128 v[230:233], v246 offset:53248
	global_load_dwordx4 v[132:135], v198, s[8:9]
	s_waitcnt lgkmcnt(12)
	v_mfma_f32_16x16x32_bf16 v[72:75], v[160:163], v[96:99], 0
	v_add_f32_e32 v220, v220, v90
	v_add_f32_e64 v221, v221, v94
	v_mfma_f32_16x16x32_bf16 v[76:79], v[160:163], v[112:115], 0
	v_add_f32_e32 v220, v220, v91
	v_add_f32_e32 v221, v221, v95
	ds_read_b128 v[234:237], v209 offset:47104
	global_load_dwordx4 v[128:131], v199, s[8:9]
	s_waitcnt lgkmcnt(11)
	v_mfma_f32_16x16x32_bf16 v[32:35], v[164:167], v[216:219], v[32:35]
	v_add_f32_e32 v194, v194, v220
	v_add_f32_e32 v195, v195, v221
	v_mfma_f32_16x16x32_bf16 v[36:39], v[164:167], v[238:241], v[36:39]
	v_exp_f32_e32 v64, v64
	ds_read_b128 v[160:163], v201 offset:57344
	global_load_dwordx4 v[152:155], v196, s[6:7]
	s_waitcnt lgkmcnt(10)
	v_mfma_f32_16x16x32_bf16 v[76:79], v[168:171], v[116:119], v[76:79]
	v_exp_f32_e32 v68, v68
	v_mfma_f32_16x16x32_bf16 v[72:75], v[168:171], v[100:103], v[72:75]
	v_exp_f32_e32 v65, v65
	ds_read_b128 v[164:167], v210 offset:32768
	global_load_dwordx4 v[156:159], v197, s[6:7]
	s_waitcnt lgkmcnt(9)
	v_mfma_f32_16x16x32_bf16 v[44:47], v[172:175], v[238:241], v[44:47]
	v_exp_f32_e32 v69, v69
	v_mfma_f32_16x16x32_bf16 v[40:43], v[172:175], v[216:219], v[40:43]
	v_exp_f32_e32 v66, v66
	ds_read_b128 v[168:171], v202 offset:57344
	s_waitcnt lgkmcnt(8)
	v_mfma_f32_16x16x32_bf16 v[72:75], v[176:179], v[104:107], v[72:75]
	v_exp_f32_e32 v70, v70
	v_mfma_f32_16x16x32_bf16 v[76:79], v[176:179], v[120:123], v[76:79]
	v_exp_f32_e64 v67, v67
	ds_read_b128 v[172:175], v210 offset:34816
	s_waitcnt lgkmcnt(7)
	v_mfma_f32_16x16x32_bf16 v[48:51], v[180:183], v[216:219], v[48:51]
	v_exp_f32_e32 v71, v71
	v_mfma_f32_16x16x32_bf16 v[52:55], v[180:183], v[238:241], v[52:55]
	v_add_f32_e32 v220, v64, v65
	ds_read_b128 v[176:179], v203 offset:57344
	s_waitcnt lgkmcnt(6)
	v_mfma_f32_16x16x32_bf16 v[76:79], v[230:233], v[124:127], v[76:79]
	v_add_f32_e64 v221, v68, v69
	v_mfma_f32_16x16x32_bf16 v[72:75], v[230:233], v[108:111], v[72:75]
	v_add_f32_e32 v220, v220, v66
	ds_read_b128 v[180:183], v210 offset:36864
	s_waitcnt lgkmcnt(6)
	v_mfma_f32_16x16x32_bf16 v[60:63], v[234:237], v[238:241], v[60:63]
	v_add_f32_e32 v221, v221, v70
	v_add_f32_e32 v220, v220, v67
	v_mfma_f32_16x16x32_bf16 v[56:59], v[234:237], v[216:219], v[56:59]
	v_add_f32_e32 v221, v221, v71
	ds_read_b128 v[230:233], v246 offset:57344
	s_waitcnt lgkmcnt(6)
	v_mfma_f32_16x16x32_bf16 v[80:83], v[160:163], v[96:99], 0
	v_exp_f32_e32 v72, v72
	v_mfma_f32_16x16x32_bf16 v[84:87], v[160:163], v[112:115], 0
	v_exp_f32_e32 v76, v76
	ds_read_b128 v[234:237], v210 offset:38912
	s_waitcnt lgkmcnt(6)
	v_mfma_f32_16x16x32_bf16 v[0:3], v[164:167], v[242:245], v[0:3]
	v_exp_f32_e32 v73, v73
	v_mfma_f32_16x16x32_bf16 v[4:7], v[164:167], v[204:207], v[4:7]
	v_exp_f32_e64 v77, v77
	ds_read_b128 v[160:163], v201 offset:61440
	s_waitcnt lgkmcnt(6)
	v_mfma_f32_16x16x32_bf16 v[84:87], v[168:171], v[116:119], v[84:87]
	v_exp_f32_e32 v74, v74
	v_mfma_f32_16x16x32_bf16 v[80:83], v[168:171], v[100:103], v[80:83]
	v_exp_f32_e32 v78, v78
	ds_read_b128 v[164:167], v210 offset:40960
	s_waitcnt lgkmcnt(6)
	v_mfma_f32_16x16x32_bf16 v[12:15], v[172:175], v[204:207], v[12:15]
	v_exp_f32_e64 v75, v75
	v_mfma_f32_16x16x32_bf16 v[8:11], v[172:175], v[242:245], v[8:11]
	v_exp_f32_e32 v79, v79
	ds_read_b128 v[168:171], v202 offset:61440
	s_waitcnt lgkmcnt(6)
	v_mfma_f32_16x16x32_bf16 v[80:83], v[176:179], v[104:107], v[80:83]
	v_add_f32_e32 v220, v220, v72
	v_add_f32_e32 v221, v221, v76
	v_mfma_f32_16x16x32_bf16 v[84:87], v[176:179], v[120:123], v[84:87]
	v_add_f32_e32 v220, v220, v73
	ds_read_b128 v[172:175], v210 offset:43008
	s_waitcnt lgkmcnt(6)
	v_mfma_f32_16x16x32_bf16 v[16:19], v[180:183], v[242:245], v[16:19]
	v_add_f32_e32 v221, v221, v77
	v_add_f32_e32 v220, v220, v74
	v_mfma_f32_16x16x32_bf16 v[20:23], v[180:183], v[204:207], v[20:23]
	v_add_f32_e64 v221, v221, v78
	ds_read_b128 v[176:179], v203 offset:61440
	s_waitcnt lgkmcnt(6)
	v_mfma_f32_16x16x32_bf16 v[84:87], v[230:233], v[124:127], v[84:87]
	v_add_f32_e32 v220, v220, v75
	v_add_f32_e64 v221, v221, v79
	v_mfma_f32_16x16x32_bf16 v[80:83], v[230:233], v[108:111], v[80:83]
	v_cvt_pk_bf16_f32 v216, v64, v65
	ds_read_b128 v[180:183], v210 offset:45056
	s_waitcnt lgkmcnt(6)
	s_nop 0
	v_mfma_f32_16x16x32_bf16 v[28:31], v[234:237], v[204:207], v[28:31]
	v_cvt_pk_bf16_f32 v217, v66, v67
	v_cvt_pk_bf16_f32 v238, v68, v69
	v_mfma_f32_16x16x32_bf16 v[24:27], v[234:237], v[242:245], v[24:27]
	v_cvt_pk_bf16_f32 v239, v70, v71
	ds_read_b128 v[230:233], v246 offset:61440
	s_waitcnt lgkmcnt(6)
	v_mfma_f32_16x16x32_bf16 v[88:91], v[160:163], v[96:99], 0
	v_exp_f32_e32 v80, v80
	v_mfma_f32_16x16x32_bf16 v[92:95], v[160:163], v[112:115], 0
	v_exp_f32_e32 v84, v84
	ds_read_b128 v[234:237], v210 offset:47104
	s_waitcnt lgkmcnt(6)
	v_mfma_f32_16x16x32_bf16 v[32:35], v[164:167], v[242:245], v[32:35]
	v_exp_f32_e32 v81, v81
	v_mfma_f32_16x16x32_bf16 v[36:39], v[164:167], v[204:207], v[36:39]
	v_exp_f32_e64 v85, v85
	ds_read_b128 v[160:163], v201 offset:0
	s_waitcnt lgkmcnt(6)
	v_mfma_f32_16x16x32_bf16 v[92:95], v[168:171], v[116:119], v[92:95]
	v_exp_f32_e32 v82, v82
	v_mfma_f32_16x16x32_bf16 v[88:91], v[168:171], v[100:103], v[88:91]
	v_exp_f32_e32 v86, v86
	ds_read_b128 v[164:167], v209 offset:49152
	s_waitcnt lgkmcnt(6)
	v_mfma_f32_16x16x32_bf16 v[44:47], v[172:175], v[204:207], v[44:47]
	v_exp_f32_e32 v83, v83
	v_mfma_f32_16x16x32_bf16 v[40:43], v[172:175], v[242:245], v[40:43]
	v_exp_f32_e64 v87, v87
	ds_read_b128 v[168:171], v202 offset:0
	s_waitcnt lgkmcnt(6)
	v_mfma_f32_16x16x32_bf16 v[88:91], v[176:179], v[104:107], v[88:91]
	v_add_f32_e32 v220, v220, v80
	v_add_f32_e64 v221, v221, v84
	v_mfma_f32_16x16x32_bf16 v[92:95], v[176:179], v[120:123], v[92:95]
	v_add_f32_e32 v220, v220, v81
	ds_read_b128 v[172:175], v209 offset:51200
	s_waitcnt lgkmcnt(6)
	v_mfma_f32_16x16x32_bf16 v[48:51], v[180:183], v[242:245], v[48:51]
	v_add_f32_e32 v221, v221, v85
	v_add_f32_e32 v220, v220, v82
	v_mfma_f32_16x16x32_bf16 v[52:55], v[180:183], v[204:207], v[52:55]
	v_add_f32_e32 v221, v221, v86
	ds_read_b128 v[176:179], v203 offset:0
	s_waitcnt lgkmcnt(6)
	v_mfma_f32_16x16x32_bf16 v[92:95], v[230:233], v[124:127], v[92:95]
	v_add_f32_e32 v220, v220, v83
	v_add_f32_e32 v221, v221, v87
	v_mfma_f32_16x16x32_bf16 v[88:91], v[230:233], v[108:111], v[88:91]
	v_cvt_pk_bf16_f32 v218, v72, v73
	ds_read_b128 v[180:183], v209 offset:53248
	s_waitcnt lgkmcnt(6)
	v_mfma_f32_16x16x32_bf16 v[60:63], v[234:237], v[204:207], v[60:63]
	v_cvt_pk_bf16_f32 v219, v74, v75
	s_nop 0
	v_cvt_pk_bf16_f32 v240, v76, v77
	v_mfma_f32_16x16x32_bf16 v[56:59], v[234:237], v[242:245], v[56:59]
	v_cvt_pk_bf16_f32 v241, v78, v79
	ds_read_b128 v[230:233], v246 offset:0
	s_cmp_eq_u32 s100, 1
	s_cbranch_scc1 .Lattn_pa3
	s_setprio 1
	s_branch .Lattn_pb3

.Lattn_pb3:
	s_waitcnt lgkmcnt(6)
	v_mfma_f32_16x16x32_bf16 v[64:67], v[160:163], v[96:99], 0
	v_exp_f32_e32 v88, v88
	v_mfma_f32_16x16x32_bf16 v[68:71], v[160:163], v[112:115], 0
	v_exp_f32_e32 v92, v92
	ds_read_b128 v[234:237], v209 offset:55296
	s_add_u32 s8, s16, 0x3bc00380
	s_addc_u32 s9, s17, 0
	s_add_u32 s6, s15, 0x23a80000
	s_addc_u32 s7, s14, 0
	s_waitcnt lgkmcnt(6)
	v_mfma_f32_16x16x32_bf16 v[0:3], v[164:167], v[216:219], v[0:3]
	s_nop 0
	v_cvt_pk_bf16_f32 v242, v80, v81
	v_mfma_f32_16x16x32_bf16 v[4:7], v[164:167], v[238:241], v[4:7]
	v_exp_f32_e32 v89, v89
	ds_read_b128 v[160:163], v201 offset:4096
	s_waitcnt vmcnt(4)
	ds_write_b128 v225, v[136:139] offset:32768
	s_waitcnt lgkmcnt(7)
	v_mfma_f32_16x16x32_bf16 v[68:71], v[168:171], v[116:119], v[68:71]
	v_exp_f32_e32 v93, v93
	v_mfma_f32_16x16x32_bf16 v[64:67], v[168:171], v[100:103], v[64:67]
	v_cvt_pk_bf16_f32 v243, v82, v83
	ds_read_b128 v[164:167], v209 offset:57344
	ds_write_b128 v226, v[140:143] offset:32768
	s_waitcnt lgkmcnt(8)
	s_nop 0
	v_mfma_f32_16x16x32_bf16 v[12:15], v[172:175], v[238:241], v[12:15]
	v_exp_f32_e32 v90, v90
	v_mfma_f32_16x16x32_bf16 v[8:11], v[172:175], v[216:219], v[8:11]
	v_exp_f32_e32 v94, v94
	ds_read_b128 v[168:171], v202 offset:4096
	ds_write_b64 v227, v[148:149] offset:16384
	s_waitcnt lgkmcnt(9)
	v_mfma_f32_16x16x32_bf16 v[64:67], v[176:179], v[104:107], v[64:67]
	v_cvt_pk_bf16_f32 v204, v84, v85
	s_nop 0
	v_mfma_f32_16x16x32_bf16 v[68:71], v[176:179], v[120:123], v[68:71]
	v_exp_f32_e32 v91, v91
	ds_read_b128 v[172:175], v209 offset:59392
	ds_write_b64 v228, v[150:151] offset:16384
	s_waitcnt lgkmcnt(10)
	v_mfma_f32_16x16x32_bf16 v[16:19], v[180:183], v[216:219], v[16:19]
	v_exp_f32_e32 v95, v95
	v_mfma_f32_16x16x32_bf16 v[20:23], v[180:183], v[238:241], v[20:23]
	v_cvt_pk_bf16_f32 v205, v86, v87
	v_add_f32_e32 v220, v220, v88
	ds_read_b128 v[176:179], v203 offset:4096
	ds_write_b64 v229, v[144:145] offset:16384
	s_waitcnt lgkmcnt(11)
	v_mfma_f32_16x16x32_bf16 v[68:71], v[230:233], v[124:127], v[68:71]
	v_add_f32_e32 v221, v221, v92
	v_add_f32_e32 v220, v220, v89
	v_mfma_f32_16x16x32_bf16 v[64:67], v[230:233], v[108:111], v[64:67]
	v_add_f32_e32 v221, v221, v93
	v_cvt_pk_bf16_f32 v244, v88, v89
	ds_read_b128 v[180:183], v209 offset:61440
	ds_write_b64 v184, v[146:147] offset:16384
	s_waitcnt lgkmcnt(12)
	v_mfma_f32_16x16x32_bf16 v[28:31], v[234:237], v[238:241], v[28:31]
	v_cvt_pk_bf16_f32 v245, v90, v91
	s_nop 0
	v_cvt_pk_bf16_f32 v206, v92, v93
	v_mfma_f32_16x16x32_bf16 v[24:27], v[234:237], v[216:219], v[24:27]
	v_cvt_pk_bf16_f32 v207, v94, v95
	ds_read_b128 v[230:233], v246 offset:4096
	global_load_dwordx4 v[148:151], v198, s[8:9]
	s_waitcnt lgkmcnt(12)
	v_mfma_f32_16x16x32_bf16 v[72:75], v[160:163], v[96:99], 0
	v_add_f32_e32 v220, v220, v90
	v_add_f32_e64 v221, v221, v94
	v_mfma_f32_16x16x32_bf16 v[76:79], v[160:163], v[112:115], 0
	v_add_f32_e32 v220, v220, v91
	v_add_f32_e32 v221, v221, v95
	ds_read_b128 v[234:237], v209 offset:63488
	global_load_dwordx4 v[144:147], v199, s[8:9]
	s_waitcnt lgkmcnt(11)
	v_mfma_f32_16x16x32_bf16 v[32:35], v[164:167], v[216:219], v[32:35]
	v_add_f32_e32 v194, v194, v220
	v_add_f32_e32 v195, v195, v221
	v_mfma_f32_16x16x32_bf16 v[36:39], v[164:167], v[238:241], v[36:39]
	v_exp_f32_e32 v64, v64
	ds_read_b128 v[160:163], v201 offset:8192
	global_load_dwordx4 v[136:139], v196, s[6:7]
	s_waitcnt lgkmcnt(10)
	v_mfma_f32_16x16x32_bf16 v[76:79], v[168:171], v[116:119], v[76:79]
	v_exp_f32_e32 v68, v68
	v_mfma_f32_16x16x32_bf16 v[72:75], v[168:171], v[100:103], v[72:75]
	v_exp_f32_e32 v65, v65
	ds_read_b128 v[164:167], v210 offset:49152
	global_load_dwordx4 v[140:143], v197, s[6:7]
	s_waitcnt lgkmcnt(9)
	v_mfma_f32_16x16x32_bf16 v[44:47], v[172:175], v[238:241], v[44:47]
	v_exp_f32_e32 v69, v69
	v_mfma_f32_16x16x32_bf16 v[40:43], v[172:175], v[216:219], v[40:43]
	v_exp_f32_e32 v66, v66
	ds_read_b128 v[168:171], v202 offset:8192
	s_waitcnt lgkmcnt(8)
	v_mfma_f32_16x16x32_bf16 v[72:75], v[176:179], v[104:107], v[72:75]
	v_exp_f32_e32 v70, v70
	v_mfma_f32_16x16x32_bf16 v[76:79], v[176:179], v[120:123], v[76:79]
	v_exp_f32_e64 v67, v67
	ds_read_b128 v[172:175], v210 offset:51200
	s_waitcnt lgkmcnt(7)
	v_mfma_f32_16x16x32_bf16 v[48:51], v[180:183], v[216:219], v[48:51]
	v_exp_f32_e32 v71, v71
	v_mfma_f32_16x16x32_bf16 v[52:55], v[180:183], v[238:241], v[52:55]
	v_add_f32_e32 v220, v64, v65
	ds_read_b128 v[176:179], v203 offset:8192
	s_waitcnt lgkmcnt(6)
	v_mfma_f32_16x16x32_bf16 v[76:79], v[230:233], v[124:127], v[76:79]
	v_add_f32_e64 v221, v68, v69
	v_mfma_f32_16x16x32_bf16 v[72:75], v[230:233], v[108:111], v[72:75]
	v_add_f32_e32 v220, v220, v66
	ds_read_b128 v[180:183], v210 offset:53248
	s_waitcnt lgkmcnt(6)
	v_mfma_f32_16x16x32_bf16 v[60:63], v[234:237], v[238:241], v[60:63]
	v_add_f32_e32 v221, v221, v70
	v_add_f32_e32 v220, v220, v67
	v_mfma_f32_16x16x32_bf16 v[56:59], v[234:237], v[216:219], v[56:59]
	v_add_f32_e32 v221, v221, v71
	ds_read_b128 v[230:233], v246 offset:8192
	s_waitcnt lgkmcnt(6)
	v_mfma_f32_16x16x32_bf16 v[80:83], v[160:163], v[96:99], 0
	v_exp_f32_e32 v72, v72
	v_mfma_f32_16x16x32_bf16 v[84:87], v[160:163], v[112:115], 0
	v_exp_f32_e32 v76, v76
	ds_read_b128 v[234:237], v210 offset:55296
	s_waitcnt lgkmcnt(6)
	v_mfma_f32_16x16x32_bf16 v[0:3], v[164:167], v[242:245], v[0:3]
	v_exp_f32_e32 v73, v73
	v_mfma_f32_16x16x32_bf16 v[4:7], v[164:167], v[204:207], v[4:7]
	v_exp_f32_e64 v77, v77
	ds_read_b128 v[160:163], v201 offset:12288
	s_waitcnt lgkmcnt(6)
	v_mfma_f32_16x16x32_bf16 v[84:87], v[168:171], v[116:119], v[84:87]
	v_exp_f32_e32 v74, v74
	v_mfma_f32_16x16x32_bf16 v[80:83], v[168:171], v[100:103], v[80:83]
	v_exp_f32_e32 v78, v78
	ds_read_b128 v[164:167], v210 offset:57344
	s_waitcnt lgkmcnt(6)
	v_mfma_f32_16x16x32_bf16 v[12:15], v[172:175], v[204:207], v[12:15]
	v_exp_f32_e64 v75, v75
	v_mfma_f32_16x16x32_bf16 v[8:11], v[172:175], v[242:245], v[8:11]
	v_exp_f32_e32 v79, v79
	ds_read_b128 v[168:171], v202 offset:12288
	s_waitcnt lgkmcnt(6)
	v_mfma_f32_16x16x32_bf16 v[80:83], v[176:179], v[104:107], v[80:83]
	v_add_f32_e32 v220, v220, v72
	v_add_f32_e32 v221, v221, v76
	v_mfma_f32_16x16x32_bf16 v[84:87], v[176:179], v[120:123], v[84:87]
	v_add_f32_e64 v220, v220, v73
	ds_read_b128 v[172:175], v210 offset:59392
	s_add_u32 s10, s10, 0x200
	s_addc_u32 s11, s11, 0
	s_add_u32 s12, s12, 0x40000
	s_addc_u32 s13, s13, 0
	s_add_i32 s4, s4, 4
	s_cmpk_lt_u32 s4, 0x104
	s_cselect_b64 s[6:7], -1, 0
	s_and_b64 s[6:7], s[0:1], s[6:7]
	s_and_b64 vcc, exec, s[6:7]
	s_waitcnt lgkmcnt(6)
	v_mfma_f32_16x16x32_bf16 v[16:19], v[180:183], v[242:245], v[16:19]
	v_add_f32_e32 v221, v221, v77
	v_add_f32_e32 v220, v220, v74
	v_mfma_f32_16x16x32_bf16 v[20:23], v[180:183], v[204:207], v[20:23]
	v_add_f32_e32 v221, v221, v78
	ds_read_b128 v[176:179], v203 offset:12288
	s_waitcnt lgkmcnt(6)
	v_mfma_f32_16x16x32_bf16 v[84:87], v[230:233], v[124:127], v[84:87]
	v_add_f32_e32 v220, v220, v75
	v_add_f32_e32 v221, v221, v79
	v_mfma_f32_16x16x32_bf16 v[80:83], v[230:233], v[108:111], v[80:83]
	v_cvt_pk_bf16_f32 v216, v64, v65
	ds_read_b128 v[180:183], v210 offset:61440
	s_waitcnt lgkmcnt(6)
	v_mfma_f32_16x16x32_bf16 v[28:31], v[234:237], v[204:207], v[28:31]
	v_cvt_pk_bf16_f32 v217, v66, v67
	v_cvt_pk_bf16_f32 v238, v68, v69
	s_nop 0
	v_mfma_f32_16x16x32_bf16 v[24:27], v[234:237], v[242:245], v[24:27]
	v_cvt_pk_bf16_f32 v239, v70, v71
	ds_read_b128 v[230:233], v246 offset:12288
	s_waitcnt lgkmcnt(6)
	s_nop 0
	v_mfma_f32_16x16x32_bf16 v[88:91], v[160:163], v[96:99], 0
	v_exp_f32_e32 v80, v80
	v_mfma_f32_16x16x32_bf16 v[92:95], v[160:163], v[112:115], 0
	v_exp_f32_e32 v84, v84
	ds_read_b128 v[234:237], v210 offset:63488
	s_waitcnt lgkmcnt(6)
	v_mfma_f32_16x16x32_bf16 v[32:35], v[164:167], v[242:245], v[32:35]
	v_exp_f32_e32 v81, v81
	v_mfma_f32_16x16x32_bf16 v[36:39], v[164:167], v[204:207], v[36:39]
	v_exp_f32_e32 v85, v85
	s_waitcnt lgkmcnt(5)
	v_mfma_f32_16x16x32_bf16 v[92:95], v[168:171], v[116:119], v[92:95]
	v_exp_f32_e32 v82, v82
	v_mfma_f32_16x16x32_bf16 v[88:91], v[168:171], v[100:103], v[88:91]
	v_exp_f32_e64 v86, v86
	s_waitcnt lgkmcnt(4)
	v_mfma_f32_16x16x32_bf16 v[44:47], v[172:175], v[204:207], v[44:47]
	v_exp_f32_e32 v83, v83
	v_mfma_f32_16x16x32_bf16 v[40:43], v[172:175], v[242:245], v[40:43]
	v_exp_f32_e64 v87, v87
	s_waitcnt lgkmcnt(3)
	v_mfma_f32_16x16x32_bf16 v[88:91], v[176:179], v[104:107], v[88:91]
	v_add_f32_e32 v220, v220, v80
	v_add_f32_e32 v221, v221, v84
	v_mfma_f32_16x16x32_bf16 v[92:95], v[176:179], v[120:123], v[92:95]
	v_add_f32_e64 v220, v220, v81
	s_waitcnt lgkmcnt(0)
	s_barrier
	ds_read_b128 v[160:163], v201 offset:16384
	ds_read_b128 v[164:167], v209 offset:0
	ds_read_b128 v[168:171], v202 offset:16384
	ds_read_b128 v[172:175], v209 offset:2048
	v_mfma_f32_16x16x32_bf16 v[48:51], v[180:183], v[242:245], v[48:51]
	v_add_f32_e32 v221, v221, v85
	v_add_f32_e32 v220, v220, v82
	v_mfma_f32_16x16x32_bf16 v[52:55], v[180:183], v[204:207], v[52:55]
	v_add_f32_e32 v221, v221, v86
	ds_read_b128 v[176:179], v203 offset:16384
	v_mfma_f32_16x16x32_bf16 v[92:95], v[230:233], v[124:127], v[92:95]
	v_add_f32_e32 v220, v220, v83
	v_add_f32_e64 v221, v221, v87
	v_mfma_f32_16x16x32_bf16 v[88:91], v[230:233], v[108:111], v[88:91]
	v_cvt_pk_bf16_f32 v218, v72, v73
	ds_read_b128 v[180:183], v209 offset:4096
	v_mfma_f32_16x16x32_bf16 v[60:63], v[234:237], v[204:207], v[60:63]
	v_cvt_pk_bf16_f32 v219, v74, v75
	v_cvt_pk_bf16_f32 v240, v76, v77
	v_mfma_f32_16x16x32_bf16 v[56:59], v[234:237], v[242:245], v[56:59]
	v_cvt_pk_bf16_f32 v241, v78, v79
	ds_read_b128 v[230:233], v246 offset:16384
	s_cbranch_vccnz .LBB0_734
	s_setprio 0
	s_waitcnt vmcnt(0)
	s_nop 7
	s_nop 7
	ds_swizzle_b32 v64, v194 offset:swizzle(SWAP,16)
	s_waitcnt lgkmcnt(0)
	v_add_f32_e32 v194, v194, v64
	v_mov_b32_e32 v65, v194
	s_nop 1
	v_permlane32_swap_b32_e32 v194, v65
	v_add_f32_e32 v194, v194, v65
	s_nop 0
	v_rcp_f32_e32 v66, v194
	ds_swizzle_b32 v64, v195 offset:swizzle(SWAP,16)
	s_waitcnt lgkmcnt(0)
	v_add_f32_e32 v195, v195, v64
	v_mov_b32_e32 v65, v195
	s_nop 1
	v_permlane32_swap_b32_e32 v195, v65
	v_add_f32_e32 v195, v195, v65
	s_nop 0
	v_rcp_f32_e32 v67, v195
	v_readlane_b32 s100, v250, 8
	v_mbcnt_lo_u32_b32 v68, -1, 0
	v_mbcnt_hi_u32_b32 v68, -1, v68
	v_and_b32_e32 v69, 15, v68
	v_lshrrev_b32_e32 v70, 4, v68
	s_lshr_b32 s101, s100, 1
	v_add_u32_e32 v69, s101, v69
	v_lshlrev_b32_e32 v69, 12, v69
	v_and_b32_e32 v71, 1, v70
	v_lshlrev_b32_e32 v71, 5, v71
	v_and_b32_e32 v70, 2, v70
	v_lshl_add_u32 v71, v70, 3, v71
	v_add_u32_e32 v70, v69, v71
	v_add_u32_e32 v71, 0x10000, v70
	v_mul_f32_e32 v0, v0, v66
	v_mul_f32_e32 v1, v1, v66
	v_mul_f32_e32 v2, v2, v66
	v_mul_f32_e32 v3, v3, v66
	v_mul_f32_e32 v8, v8, v66
	v_mul_f32_e32 v9, v9, v66
	v_mul_f32_e32 v10, v10, v66
	v_mul_f32_e32 v11, v11, v66
	v_cvt_pk_bf16_f32 v72, v0, v1
	v_cvt_pk_bf16_f32 v73, v2, v3
	v_cvt_pk_bf16_f32 v74, v8, v9
	v_cvt_pk_bf16_f32 v75, v10, v11
	s_nop 1
	v_permlane16_swap_b32_e32 v72, v74
	v_permlane16_swap_b32_e32 v73, v75
	s_nop 1
	global_store_dwordx4 v70, v[72:75], s[58:59] offset:0
	v_mul_f32_e32 v16, v16, v66
	v_mul_f32_e32 v17, v17, v66
	v_mul_f32_e32 v18, v18, v66
	v_mul_f32_e32 v19, v19, v66
	v_mul_f32_e32 v24, v24, v66
	v_mul_f32_e32 v25, v25, v66
	v_mul_f32_e32 v26, v26, v66
	v_mul_f32_e32 v27, v27, v66
	v_cvt_pk_bf16_f32 v76, v16, v17
	v_cvt_pk_bf16_f32 v77, v18, v19
	v_cvt_pk_bf16_f32 v78, v24, v25
	v_cvt_pk_bf16_f32 v79, v26, v27
	s_nop 1
	v_permlane16_swap_b32_e32 v76, v78
	v_permlane16_swap_b32_e32 v77, v79
	s_nop 1
	global_store_dwordx4 v70, v[76:79], s[58:59] offset:64
	v_mul_f32_e32 v32, v32, v66
	v_mul_f32_e32 v33, v33, v66
	v_mul_f32_e32 v34, v34, v66
	v_mul_f32_e32 v35, v35, v66
	v_mul_f32_e32 v40, v40, v66
	v_mul_f32_e32 v41, v41, v66
	v_mul_f32_e32 v42, v42, v66
	v_mul_f32_e32 v43, v43, v66
	v_cvt_pk_bf16_f32 v80, v32, v33
	v_cvt_pk_bf16_f32 v81, v34, v35
	v_cvt_pk_bf16_f32 v82, v40, v41
	v_cvt_pk_bf16_f32 v83, v42, v43
	s_nop 1
	v_permlane16_swap_b32_e32 v80, v82
	v_permlane16_swap_b32_e32 v81, v83
	s_nop 1
	global_store_dwordx4 v70, v[80:83], s[58:59] offset:128
	v_mul_f32_e32 v48, v48, v66
	v_mul_f32_e32 v49, v49, v66
	v_mul_f32_e32 v50, v50, v66
	v_mul_f32_e32 v51, v51, v66
	v_mul_f32_e32 v56, v56, v66
	v_mul_f32_e32 v57, v57, v66
	v_mul_f32_e32 v58, v58, v66
	v_mul_f32_e32 v59, v59, v66
	v_cvt_pk_bf16_f32 v84, v48, v49
	v_cvt_pk_bf16_f32 v85, v50, v51
	v_cvt_pk_bf16_f32 v86, v56, v57
	v_cvt_pk_bf16_f32 v87, v58, v59
	s_nop 1
	v_permlane16_swap_b32_e32 v84, v86
	v_permlane16_swap_b32_e32 v85, v87
	s_nop 1
	global_store_dwordx4 v70, v[84:87], s[58:59] offset:192
	v_mul_f32_e32 v4, v4, v67
	v_mul_f32_e32 v5, v5, v67
	v_mul_f32_e32 v6, v6, v67
	v_mul_f32_e32 v7, v7, v67
	v_mul_f32_e32 v12, v12, v67
	v_mul_f32_e32 v13, v13, v67
	v_mul_f32_e32 v14, v14, v67
	v_mul_f32_e32 v15, v15, v67
	v_cvt_pk_bf16_f32 v88, v4, v5
	v_cvt_pk_bf16_f32 v89, v6, v7
	v_cvt_pk_bf16_f32 v90, v12, v13
	v_cvt_pk_bf16_f32 v91, v14, v15
	s_nop 1
	v_permlane16_swap_b32_e32 v88, v90
	v_permlane16_swap_b32_e32 v89, v91
	s_nop 1
	global_store_dwordx4 v71, v[88:91], s[58:59] offset:0
	v_mul_f32_e32 v20, v20, v67
	v_mul_f32_e32 v21, v21, v67
	v_mul_f32_e32 v22, v22, v67
	v_mul_f32_e32 v23, v23, v67
	v_mul_f32_e32 v28, v28, v67
	v_mul_f32_e32 v29, v29, v67
	v_mul_f32_e32 v30, v30, v67
	v_mul_f32_e32 v31, v31, v67
	v_cvt_pk_bf16_f32 v92, v20, v21
	v_cvt_pk_bf16_f32 v93, v22, v23
	v_cvt_pk_bf16_f32 v94, v28, v29
	v_cvt_pk_bf16_f32 v95, v30, v31
	s_nop 1
	v_permlane16_swap_b32_e32 v92, v94
	v_permlane16_swap_b32_e32 v93, v95
	s_nop 1
	global_store_dwordx4 v71, v[92:95], s[58:59] offset:64
	v_mul_f32_e32 v36, v36, v67
	v_mul_f32_e32 v37, v37, v67
	v_mul_f32_e32 v38, v38, v67
	v_mul_f32_e32 v39, v39, v67
	v_mul_f32_e32 v44, v44, v67
	v_mul_f32_e32 v45, v45, v67
	v_mul_f32_e32 v46, v46, v67
	v_mul_f32_e32 v47, v47, v67
	v_cvt_pk_bf16_f32 v72, v36, v37
	v_cvt_pk_bf16_f32 v73, v38, v39
	v_cvt_pk_bf16_f32 v74, v44, v45
	v_cvt_pk_bf16_f32 v75, v46, v47
	s_nop 1
	v_permlane16_swap_b32_e32 v72, v74
	v_permlane16_swap_b32_e32 v73, v75
	s_nop 1
	global_store_dwordx4 v71, v[72:75], s[58:59] offset:128
	v_mul_f32_e32 v52, v52, v67
	v_mul_f32_e32 v53, v53, v67
	v_mul_f32_e32 v54, v54, v67
	v_mul_f32_e32 v55, v55, v67
	v_mul_f32_e32 v60, v60, v67
	v_mul_f32_e32 v61, v61, v67
	v_mul_f32_e32 v62, v62, v67
	v_mul_f32_e32 v63, v63, v67
	v_cvt_pk_bf16_f32 v76, v52, v53
	v_cvt_pk_bf16_f32 v77, v54, v55
	v_cvt_pk_bf16_f32 v78, v60, v61
	v_cvt_pk_bf16_f32 v79, v62, v63
	s_nop 1
	v_permlane16_swap_b32_e32 v76, v78
	v_permlane16_swap_b32_e32 v77, v79
	s_nop 1
	global_store_dwordx4 v71, v[76:79], s[58:59] offset:192
	s_barrier
